# expert-weight converter WGs throttled (s_sleep 30 per k-block) to lower memory pressure on the in-projection GEMM beside it
# speedup vs baseline: 1.0066x; 1.0066x over previous
; DI s16x4 tr16(const LAS unsigned char* p) { return __builtin_bit_cast(s16x4, __builtin_amdgcn_ds_read_tr16_b64_v4i16((LAS v4i16_t*)p)); }
; #define LDS_WAIT() asm volatile("s_waitcnt lgkmcnt(0)" ::: "memory")
; #define P0S_LOAD(dst, krow0) do { _Pragma("unroll") for (int i = 0; i < 16; ++i) dst[i] = *(const f32x4*)(wp + (size_t)((krow0) + 2 * i) * ld); } while (0)
; #define P0S_PUT(src, r0) do { _Pragma("unroll") for (int i = 0; i < 16; ++i) { \
;         u32x2 pk; pk.x = cvtpk(src[i][0], src[i][1]) + 0x02800280u; pk.y = cvtpk(src[i][2], src[i][3]) + 0x02800280u;        \
;         *(LAS u32x2*)(img + wb[i & 7] + ((r0) / 16 + (i >> 3)) * 4096) = pk; } } while (0)
; #define P0S_F8(lo, hi) pk4_fp8m(__uint_as_float((lo) << 16), __uint_as_float((lo) & 0xffff0000u), __uint_as_float((hi) << 16), __uint_as_float((hi) & 0xffff0000u))
; template <int MODE>
; DI void p0_strip_fp8(const float* W, int ld, unsigned char* WT, int K, int n0, LAS unsigned char* img, int lane) {
;     ...
;     P0S_LOAD(va, 0);
; #pragma unroll 1
;     for (int kb = 0; kb < 32; ++kb) {
;         P0S_LOAD(vb, 64 * kb + 32);
;         P0S_PUT(va, 0);
;         if (kb < 31) P0S_LOAD(va, 64 * kb + 64);
;         P0S_PUT(vb, 32);
;         LDS_WAIT();
; #pragma unroll 2
;         for (int nb = 0; nb < 8; ++nb) {
;             const s16x4 t0 = tr16(img + rb[0] + 32 * (nb ^ cx[0])), t1 = tr16(img + rb[1] + 32 * (nb ^ cx[1])), t2 = tr16(img + rb[2] + 32 * (nb ^ cx[2])), t3 = tr16(img + rb[3] + 32 * (nb ^ cx[3]));
;             const u32x2 f0 = __builtin_bit_cast(u32x2, t0), f1 = __builtin_bit_cast(u32x2, t1), f2 = __builtin_bit_cast(u32x2, t2), f3 = __builtin_bit_cast(u32x2, t3);
;             u32x4 o; o.x = P0S_F8(f0.x, f0.y); o.y = P0S_F8(f1.x, f1.y); o.z = P0S_F8(f2.x, f2.y); o.w = P0S_F8(f3.x, f3.y);
;             *(u32x4*)(WT + (size_t)(unsigned)orow[nb] + 64 * kb) = o; }
;         LDS_WAIT();
;     }
.LBB0_281:
	v_xor_b32_e32 v82, s2, v150
	v_xor_b32_e32 v83, s2, v151
	s_cmp_eq_u32 s2, 1
	v_lshlrev_b32_e32 v82, 5, v82
	v_lshlrev_b32_e32 v83, 5, v83
	s_cselect_b64 vcc, -1, 0
	s_cmp_eq_u32 s2, 2
	v_cndmask_b32_e32 v84, v2, v1, vcc
	v_add_u32_e32 v85, v152, v82
	v_add_u32_e32 v86, v153, v82
	v_add_u32_e32 v87, v152, v83
	v_add_u32_e32 v88, v153, v83
	s_cselect_b64 vcc, -1, 0
	s_cmp_eq_u32 s2, 3
	v_cndmask_b32_e32 v90, v84, v4, vcc
	ds_read_b64_tr_b16 v[82:83], v85
	ds_read_b64_tr_b16 v[84:85], v86 offset:1024
	ds_read_b64_tr_b16 v[86:87], v87 offset:2048
	ds_read_b64_tr_b16 v[88:89], v88 offset:3072
	s_cselect_b64 vcc, -1, 0
	s_cmp_eq_u32 s2, 4
	v_cndmask_b32_e32 v90, v90, v3, vcc
	s_cselect_b64 vcc, -1, 0
	s_cmp_eq_u32 s2, 5
	v_cndmask_b32_e32 v90, v90, v6, vcc
	s_cselect_b64 vcc, -1, 0
	s_cmp_eq_u32 s2, 6
	v_cndmask_b32_e32 v90, v90, v5, vcc
	s_cselect_b64 vcc, -1, 0
	s_cmp_eq_u32 s2, 7
	v_cndmask_b32_e32 v90, v90, v8, vcc
	s_cselect_b64 vcc, -1, 0
	s_add_i32 s63, s2, 1
	s_waitcnt lgkmcnt(3)
	v_lshlrev_b32_e32 v91, 16, v82
	v_and_b32_e32 v82, 0xffff0000, v82
	v_lshlrev_b32_e32 v92, 16, v83
	v_and_b32_e32 v83, 0xffff0000, v83
	s_waitcnt lgkmcnt(2)
	v_lshlrev_b32_e32 v93, 16, v84
	v_and_b32_e32 v84, 0xffff0000, v84
	v_lshlrev_b32_e32 v94, 16, v85
	v_and_b32_e32 v85, 0xffff0000, v85
	s_waitcnt lgkmcnt(1)
	v_lshlrev_b32_e32 v95, 16, v86
	v_and_b32_e32 v86, 0xffff0000, v86
	v_lshlrev_b32_e32 v96, 16, v87
	v_and_b32_e32 v87, 0xffff0000, v87
	s_waitcnt lgkmcnt(0)
	v_lshlrev_b32_e32 v97, 16, v88
	v_and_b32_e32 v88, 0xffff0000, v88
	v_lshlrev_b32_e32 v98, 16, v89
	v_and_b32_e32 v89, 0xffff0000, v89
	v_xor_b32_e32 v99, s63, v150
	v_xor_b32_e32 v100, s63, v151
	v_mov_b32_e32 v74, 0
	v_mov_b32_e32 v75, 0
	v_mov_b32_e32 v76, 0
	v_mov_b32_e32 v77, 0
	v_med3_f32 v91, v91, s52, v163
	v_med3_f32 v82, v82, s52, v163
	v_med3_f32 v101, v83, s52, v163
	v_med3_f32 v83, v93, s52, v163
	v_med3_f32 v84, v84, s52, v163
	v_med3_f32 v93, v94, s52, v163
	v_med3_f32 v94, v85, s52, v163
	v_med3_f32 v85, v95, s52, v163
	v_med3_f32 v86, v86, s52, v163
	v_med3_f32 v95, v96, s52, v163
	v_med3_f32 v96, v87, s52, v163
	v_med3_f32 v87, v97, s52, v163
	v_med3_f32 v88, v88, s52, v163
	v_med3_f32 v97, v98, s52, v163
	v_med3_f32 v98, v89, s52, v163
	v_lshlrev_b32_e32 v89, 5, v99
	v_lshlrev_b32_e32 v99, 5, v100
	v_cvt_pk_fp8_f32 v74, v91, v82
	v_cvt_pk_fp8_f32 v75, v83, v84
	v_cvt_pk_fp8_f32 v76, v85, v86
	v_cvt_pk_fp8_f32 v77, v87, v88
	v_add_u32_e32 v82, v152, v89
	v_add_u32_e32 v84, v153, v89
	v_add_u32_e32 v86, v152, v99
	v_add_u32_e32 v88, v153, v99
	ds_read_b64_tr_b16 v[82:83], v82
	ds_read_b64_tr_b16 v[84:85], v84 offset:1024
	ds_read_b64_tr_b16 v[86:87], v86 offset:2048
	ds_read_b64_tr_b16 v[88:89], v88 offset:3072
	v_med3_f32 v92, v92, s52, v163
	s_cmp_eq_u32 s63, 1
	v_cvt_pk_fp8_f32 v74, v92, v101 op_sel:[0,0,1]
	v_cvt_pk_fp8_f32 v75, v93, v94 op_sel:[0,0,1]
	v_cvt_pk_fp8_f32 v76, v95, v96 op_sel:[0,0,1]
	v_cvt_pk_fp8_f32 v77, v97, v98 op_sel:[0,0,1]
	s_waitcnt lgkmcnt(3)
	v_lshlrev_b32_e32 v92, 16, v82
	v_and_b32_e32 v82, 0xffff0000, v82
	s_waitcnt lgkmcnt(2)
	v_lshlrev_b32_e32 v94, 16, v84
	v_and_b32_e32 v84, 0xffff0000, v84
	s_waitcnt lgkmcnt(1)
	v_lshlrev_b32_e32 v96, 16, v86
	v_and_b32_e32 v86, 0xffff0000, v86
	s_waitcnt lgkmcnt(0)
	v_lshlrev_b32_e32 v98, 16, v88
	v_and_b32_e32 v88, 0xffff0000, v88
	v_mov_b32_e32 v78, 0
	v_mov_b32_e32 v79, 0
	v_mov_b32_e32 v80, 0
	v_mov_b32_e32 v81, 0
	v_cndmask_b32_e32 v90, v90, v7, vcc
	s_cselect_b64 vcc, -1, 0
	s_cmp_eq_u32 s63, 2
	v_med3_f32 v92, v92, s52, v163
	v_med3_f32 v82, v82, s52, v163
	v_med3_f32 v94, v94, s52, v163
	v_med3_f32 v84, v84, s52, v163
	v_med3_f32 v96, v96, s52, v163
	v_med3_f32 v86, v86, s52, v163
	v_med3_f32 v98, v98, s52, v163
	v_med3_f32 v88, v88, s52, v163
	v_cndmask_b32_e32 v100, v2, v1, vcc
	s_cselect_b64 vcc, -1, 0
	s_cmp_eq_u32 s63, 3
	v_cvt_pk_fp8_f32 v78, v92, v82
	v_cvt_pk_fp8_f32 v79, v94, v84
	v_cvt_pk_fp8_f32 v80, v96, v86
	v_cvt_pk_fp8_f32 v81, v98, v88
	v_cndmask_b32_e32 v91, v100, v4, vcc
	s_cselect_b64 vcc, -1, 0
	s_cmp_eq_u32 s63, 4
	v_cndmask_b32_e32 v91, v91, v3, vcc
	s_cselect_b64 vcc, -1, 0
	s_cmp_eq_u32 s63, 5
	v_lshlrev_b32_e32 v93, 16, v83
	v_and_b32_e32 v83, 0xffff0000, v83
	v_lshlrev_b32_e32 v95, 16, v85
	v_and_b32_e32 v85, 0xffff0000, v85
	v_lshlrev_b32_e32 v97, 16, v87
	v_and_b32_e32 v87, 0xffff0000, v87
	v_lshlrev_b32_e32 v99, 16, v89
	v_and_b32_e32 v89, 0xffff0000, v89
	v_cndmask_b32_e32 v91, v91, v6, vcc
	s_cselect_b64 vcc, -1, 0
	s_cmp_eq_u32 s63, 6
	v_med3_f32 v93, v93, s52, v163
	v_med3_f32 v83, v83, s52, v163
	v_med3_f32 v95, v95, s52, v163
	v_med3_f32 v85, v85, s52, v163
	v_med3_f32 v97, v97, s52, v163
	v_med3_f32 v87, v87, s52, v163
	v_med3_f32 v99, v99, s52, v163
	v_med3_f32 v89, v89, s52, v163
	v_cndmask_b32_e32 v91, v91, v5, vcc
	s_cselect_b64 vcc, -1, 0
	s_cmp_eq_u32 s63, 7
	v_cvt_pk_fp8_f32 v78, v93, v83 op_sel:[0,0,1]
	v_cvt_pk_fp8_f32 v79, v95, v85 op_sel:[0,0,1]
	v_cvt_pk_fp8_f32 v80, v97, v87 op_sel:[0,0,1]
	v_cvt_pk_fp8_f32 v81, v99, v89 op_sel:[0,0,1]
	v_cndmask_b32_e32 v91, v91, v8, vcc
	s_cselect_b64 vcc, -1, 0
	s_add_i32 s2, s2, 2
	s_cmp_eq_u32 s2, 8
	v_cndmask_b32_e32 v91, v91, v7, vcc
	global_store_dwordx4 v90, v[74:77], s[6:7]
	global_store_dwordx4 v91, v[78:81], s[6:7]
	s_cbranch_scc0 .LBB0_281
	s_sleep 30
	s_waitcnt lgkmcnt(0)
	s_add_i32 s62, s62, 1
	s_cmp_eq_u32 s62, 32
	s_cbranch_scc0 .LBB0_278
	s_mov_b64 s[0:1], 0

; DI s16x4 tr16(const LAS unsigned char* p) { return __builtin_bit_cast(s16x4, __builtin_amdgcn_ds_read_tr16_b64_v4i16((LAS v4i16_t*)p)); }
; #define LDS_WAIT() asm volatile("s_waitcnt lgkmcnt(0)" ::: "memory")
; #define P0S_LOAD(dst, krow0) do { _Pragma("unroll") for (int i = 0; i < 16; ++i) dst[i] = *(const f32x4*)(wp + (size_t)((krow0) + 2 * i) * ld); } while (0)
; #define P0S_PUT(src, r0) do { _Pragma("unroll") for (int i = 0; i < 16; ++i) { \
;         u32x2 pk; pk.x = cvtpk(src[i][0], src[i][1]) + 0x02800280u; pk.y = cvtpk(src[i][2], src[i][3]) + 0x02800280u;        \
;         *(LAS u32x2*)(img + wb[i & 7] + ((r0) / 16 + (i >> 3)) * 4096) = pk; } } while (0)
; #define P0S_F8(lo, hi) pk4_fp8m(__uint_as_float((lo) << 16), __uint_as_float((lo) & 0xffff0000u), __uint_as_float((hi) << 16), __uint_as_float((hi) & 0xffff0000u))
; template <int MODE>
; DI void p0_strip_fp8(const float* W, int ld, unsigned char* WT, int K, int n0, LAS unsigned char* img, int lane) {
;     ...
;     P0S_LOAD(va, 0);
; #pragma unroll 1
;     for (int kb = 0; kb < 32; ++kb) {
;         P0S_LOAD(vb, 64 * kb + 32);
;         P0S_PUT(va, 0);
;         if (kb < 31) P0S_LOAD(va, 64 * kb + 64);
;         P0S_PUT(vb, 32);
;         LDS_WAIT();
; #pragma unroll 2
;         for (int nb = 0; nb < 8; ++nb) {
;             const s16x4 t0 = tr16(img + rb[0] + 32 * (nb ^ cx[0])), t1 = tr16(img + rb[1] + 32 * (nb ^ cx[1])), t2 = tr16(img + rb[2] + 32 * (nb ^ cx[2])), t3 = tr16(img + rb[3] + 32 * (nb ^ cx[3]));
;             const u32x2 f0 = __builtin_bit_cast(u32x2, t0), f1 = __builtin_bit_cast(u32x2, t1), f2 = __builtin_bit_cast(u32x2, t2), f3 = __builtin_bit_cast(u32x2, t3);
;             u32x4 o; o.x = P0S_F8(f0.x, f0.y); o.y = P0S_F8(f1.x, f1.y); o.z = P0S_F8(f2.x, f2.y); o.w = P0S_F8(f3.x, f3.y);
;             *(u32x4*)(WT + (size_t)(unsigned)orow[nb] + 64 * kb) = o; }
;         LDS_WAIT();
;     }
.LBB0_289:
	v_xor_b32_e32 v82, s2, v150
	v_xor_b32_e32 v83, s2, v151
	s_cmp_eq_u32 s2, 1
	v_lshlrev_b32_e32 v82, 5, v82
	v_lshlrev_b32_e32 v83, 5, v83
	s_cselect_b64 vcc, -1, 0
	s_cmp_eq_u32 s2, 2
	v_cndmask_b32_e32 v84, v2, v1, vcc
	v_add_u32_e32 v85, v152, v82
	v_add_u32_e32 v86, v153, v82
	v_add_u32_e32 v87, v152, v83
	v_add_u32_e32 v88, v153, v83
	s_cselect_b64 vcc, -1, 0
	s_cmp_eq_u32 s2, 3
	v_cndmask_b32_e32 v90, v84, v4, vcc
	ds_read_b64_tr_b16 v[82:83], v85
	ds_read_b64_tr_b16 v[84:85], v86 offset:1024
	ds_read_b64_tr_b16 v[86:87], v87 offset:2048
	ds_read_b64_tr_b16 v[88:89], v88 offset:3072
	s_cselect_b64 vcc, -1, 0
	s_cmp_eq_u32 s2, 4
	v_cndmask_b32_e32 v90, v90, v3, vcc
	s_cselect_b64 vcc, -1, 0
	s_cmp_eq_u32 s2, 5
	v_cndmask_b32_e32 v90, v90, v6, vcc
	s_cselect_b64 vcc, -1, 0
	s_cmp_eq_u32 s2, 6
	v_cndmask_b32_e32 v90, v90, v5, vcc
	s_cselect_b64 vcc, -1, 0
	s_cmp_eq_u32 s2, 7
	v_cndmask_b32_e32 v90, v90, v8, vcc
	s_cselect_b64 vcc, -1, 0
	s_add_i32 s62, s2, 1
	s_waitcnt lgkmcnt(3)
	v_lshlrev_b32_e32 v91, 16, v82
	v_and_b32_e32 v82, 0xffff0000, v82
	v_lshlrev_b32_e32 v92, 16, v83
	v_and_b32_e32 v83, 0xffff0000, v83
	s_waitcnt lgkmcnt(2)
	v_lshlrev_b32_e32 v93, 16, v84
	v_and_b32_e32 v84, 0xffff0000, v84
	v_lshlrev_b32_e32 v94, 16, v85
	v_and_b32_e32 v85, 0xffff0000, v85
	s_waitcnt lgkmcnt(1)
	v_lshlrev_b32_e32 v95, 16, v86
	v_and_b32_e32 v86, 0xffff0000, v86
	v_lshlrev_b32_e32 v96, 16, v87
	v_and_b32_e32 v87, 0xffff0000, v87
	s_waitcnt lgkmcnt(0)
	v_lshlrev_b32_e32 v97, 16, v88
	v_and_b32_e32 v88, 0xffff0000, v88
	v_lshlrev_b32_e32 v98, 16, v89
	v_and_b32_e32 v89, 0xffff0000, v89
	v_xor_b32_e32 v99, s62, v150
	v_xor_b32_e32 v100, s62, v151
	v_mov_b32_e32 v74, 0
	v_mov_b32_e32 v75, 0
	v_mov_b32_e32 v76, 0
	v_mov_b32_e32 v77, 0
	v_med3_f32 v91, v91, s52, v163
	v_med3_f32 v82, v82, s52, v163
	v_med3_f32 v101, v83, s52, v163
	v_med3_f32 v83, v93, s52, v163
	v_med3_f32 v84, v84, s52, v163
	v_med3_f32 v93, v94, s52, v163
	v_med3_f32 v94, v85, s52, v163
	v_med3_f32 v85, v95, s52, v163
	v_med3_f32 v86, v86, s52, v163
	v_med3_f32 v95, v96, s52, v163
	v_med3_f32 v96, v87, s52, v163
	v_med3_f32 v87, v97, s52, v163
	v_med3_f32 v88, v88, s52, v163
	v_med3_f32 v97, v98, s52, v163
	v_med3_f32 v98, v89, s52, v163
	v_lshlrev_b32_e32 v89, 5, v99
	v_lshlrev_b32_e32 v99, 5, v100
	v_cvt_pk_fp8_f32 v74, v91, v82
	v_cvt_pk_fp8_f32 v75, v83, v84
	v_cvt_pk_fp8_f32 v76, v85, v86
	v_cvt_pk_fp8_f32 v77, v87, v88
	v_add_u32_e32 v82, v152, v89
	v_add_u32_e32 v84, v153, v89
	v_add_u32_e32 v86, v152, v99
	v_add_u32_e32 v88, v153, v99
	ds_read_b64_tr_b16 v[82:83], v82
	ds_read_b64_tr_b16 v[84:85], v84 offset:1024
	ds_read_b64_tr_b16 v[86:87], v86 offset:2048
	ds_read_b64_tr_b16 v[88:89], v88 offset:3072
	v_med3_f32 v92, v92, s52, v163
	s_cmp_eq_u32 s62, 1
	v_cvt_pk_fp8_f32 v74, v92, v101 op_sel:[0,0,1]
	v_cvt_pk_fp8_f32 v75, v93, v94 op_sel:[0,0,1]
	v_cvt_pk_fp8_f32 v76, v95, v96 op_sel:[0,0,1]
	v_cvt_pk_fp8_f32 v77, v97, v98 op_sel:[0,0,1]
	s_waitcnt lgkmcnt(3)
	v_lshlrev_b32_e32 v92, 16, v82
	v_and_b32_e32 v82, 0xffff0000, v82
	s_waitcnt lgkmcnt(2)
	v_lshlrev_b32_e32 v94, 16, v84
	v_and_b32_e32 v84, 0xffff0000, v84
	s_waitcnt lgkmcnt(1)
	v_lshlrev_b32_e32 v96, 16, v86
	v_and_b32_e32 v86, 0xffff0000, v86
	s_waitcnt lgkmcnt(0)
	v_lshlrev_b32_e32 v98, 16, v88
	v_and_b32_e32 v88, 0xffff0000, v88
	v_mov_b32_e32 v78, 0
	v_mov_b32_e32 v79, 0
	v_mov_b32_e32 v80, 0
	v_mov_b32_e32 v81, 0
	v_cndmask_b32_e32 v90, v90, v7, vcc
	s_cselect_b64 vcc, -1, 0
	s_cmp_eq_u32 s62, 2
	v_med3_f32 v92, v92, s52, v163
	v_med3_f32 v82, v82, s52, v163
	v_med3_f32 v94, v94, s52, v163
	v_med3_f32 v84, v84, s52, v163
	v_med3_f32 v96, v96, s52, v163
	v_med3_f32 v86, v86, s52, v163
	v_med3_f32 v98, v98, s52, v163
	v_med3_f32 v88, v88, s52, v163
	v_cndmask_b32_e32 v100, v2, v1, vcc
	s_cselect_b64 vcc, -1, 0
	s_cmp_eq_u32 s62, 3
	v_cvt_pk_fp8_f32 v78, v92, v82
	v_cvt_pk_fp8_f32 v79, v94, v84
	v_cvt_pk_fp8_f32 v80, v96, v86
	v_cvt_pk_fp8_f32 v81, v98, v88
	v_cndmask_b32_e32 v91, v100, v4, vcc
	s_cselect_b64 vcc, -1, 0
	s_cmp_eq_u32 s62, 4
	v_cndmask_b32_e32 v91, v91, v3, vcc
	s_cselect_b64 vcc, -1, 0
	s_cmp_eq_u32 s62, 5
	v_lshlrev_b32_e32 v93, 16, v83
	v_and_b32_e32 v83, 0xffff0000, v83
	v_lshlrev_b32_e32 v95, 16, v85
	v_and_b32_e32 v85, 0xffff0000, v85
	v_lshlrev_b32_e32 v97, 16, v87
	v_and_b32_e32 v87, 0xffff0000, v87
	v_lshlrev_b32_e32 v99, 16, v89
	v_and_b32_e32 v89, 0xffff0000, v89
	v_cndmask_b32_e32 v91, v91, v6, vcc
	s_cselect_b64 vcc, -1, 0
	s_cmp_eq_u32 s62, 6
	v_med3_f32 v93, v93, s52, v163
	v_med3_f32 v83, v83, s52, v163
	v_med3_f32 v95, v95, s52, v163
	v_med3_f32 v85, v85, s52, v163
	v_med3_f32 v97, v97, s52, v163
	v_med3_f32 v87, v87, s52, v163
	v_med3_f32 v99, v99, s52, v163
	v_med3_f32 v89, v89, s52, v163
	v_cndmask_b32_e32 v91, v91, v5, vcc
	s_cselect_b64 vcc, -1, 0
	s_cmp_eq_u32 s62, 7
	v_cvt_pk_fp8_f32 v78, v93, v83 op_sel:[0,0,1]
	v_cvt_pk_fp8_f32 v79, v95, v85 op_sel:[0,0,1]
	v_cvt_pk_fp8_f32 v80, v97, v87 op_sel:[0,0,1]
	v_cvt_pk_fp8_f32 v81, v99, v89 op_sel:[0,0,1]
	v_cndmask_b32_e32 v91, v91, v8, vcc
	s_cselect_b64 vcc, -1, 0
	s_add_i32 s2, s2, 2
	s_cmp_eq_u32 s2, 8
	v_cndmask_b32_e32 v91, v91, v7, vcc
	global_store_dwordx4 v90, v[74:77], s[6:7]
	global_store_dwordx4 v91, v[78:81], s[6:7]
	s_cbranch_scc0 .LBB0_289
	s_sleep 30
	s_waitcnt lgkmcnt(0)
	s_add_i32 s61, s61, 1
	s_cmp_eq_u32 s61, 32
	s_cbranch_scc0 .LBB0_286
	s_branch .LBB0_275
